# baseline (speedup 1.0000x reference)
_Z11proj_kernelPKfS0_PKDF16_S0_S0_PDF16_S3_:
	s_load_dwordx8 s[4:11], s[0:1], 0x0
	s_load_dwordx2 s[16:17], s[0:1], 0x20
	v_readfirstlane_b32 s15, v0
	s_lshl_b32 s3, s2, 6
	s_add_i32 s12, s3, 0xffffe000
	s_ashr_i32 s13, s3, 31
	s_cmpk_lt_i32 s3, 0x2000
	s_cselect_b32 s13, s13, 0
	s_cselect_b32 s12, s3, s12
	s_waitcnt lgkmcnt(0)
	s_cselect_b32 s3, s5, s7
	s_cselect_b32 s6, s4, s6
	s_lshl_b64 s[4:5], s[12:13], 10
	s_add_u32 s4, s6, s4
	s_addc_u32 s5, s3, s5
	s_lshr_b32 s15, s15, 6
	s_cmp_lt_u32 s15, 4
	s_cselect_b32 s18, s10, s16
	s_cselect_b32 s19, s11, s17
	s_and_b32 s15, s15, 3
	s_lshl_b32 s15, s15, 8
	s_add_u32 s18, s18, s15
	s_addc_u32 s19, s19, 0
	v_bfe_u32 v204, v0, 5, 1
	v_lshlrev_b32_e32 v204, 4, v204
	global_load_dwordx4 v[172:175], v204, s[18:19]
	global_load_dwordx4 v[176:179], v204, s[18:19] offset:32
	global_load_dwordx4 v[180:183], v204, s[18:19] offset:64
	global_load_dwordx4 v[184:187], v204, s[18:19] offset:96
	global_load_dwordx4 v[188:191], v204, s[18:19] offset:128
	global_load_dwordx4 v[192:195], v204, s[18:19] offset:160
	global_load_dwordx4 v[196:199], v204, s[18:19] offset:192
	global_load_dwordx4 v[200:203], v204, s[18:19] offset:224
	v_lshlrev_b32_e32 v70, 4, v0
	v_mov_b32_e32 v71, 0
	s_movk_i32 s14, 0x2000
	v_lshl_add_u64 v[26:27], s[4:5], 0, v[70:71]
	v_add_co_u32_e32 v10, vcc, s14, v26
	s_movk_i32 s3, 0x6000
	s_nop 0
	v_addc_co_u32_e32 v11, vcc, 0, v27, vcc
	v_add_co_u32_e32 v18, vcc, s3, v26
	s_mov_b32 s6, 0xa000
	s_nop 0
	v_addc_co_u32_e32 v19, vcc, 0, v27, vcc
	v_or_b32_e32 v42, 0x400, v0
	v_add_co_u32_e32 v28, vcc, s6, v26
	v_lshlrev_b32_e32 v1, 4, v42
	v_or_b32_e32 v43, 0x800, v0
	v_addc_co_u32_e32 v29, vcc, 0, v27, vcc
	s_mov_b32 s6, 0xe000
	global_load_dwordx4 v[2:5], v[10:11], off
	global_load_dwordx4 v[6:9], v1, s[4:5]
	v_lshlrev_b32_e32 v1, 4, v43
	v_or_b32_e32 v44, 0xc00, v0
	v_add_co_u32_e32 v34, vcc, s6, v26
	global_load_dwordx4 v[10:13], v[18:19], off
	global_load_dwordx4 v[14:17], v1, s[4:5]
	v_lshlrev_b32_e32 v1, 4, v44
	global_load_dwordx4 v[18:21], v[28:29], off
	global_load_dwordx4 v[22:25], v1, s[4:5]
	v_addc_co_u32_e32 v35, vcc, 0, v27, vcc
	global_load_dwordx4 v[26:29], v70, s[4:5]
	global_load_dwordx4 v[30:33], v[34:35], off
	s_load_dwordx4 s[4:7], s[0:1], 0x20
	s_load_dwordx2 s[12:13], s[0:1], 0x30
	v_and_b32_e32 v73, 63, v0
	v_and_b32_e32 v1, 31, v0
	v_lshrrev_b32_e32 v76, 6, v0
	v_bfe_u32 v77, v0, 5, 1
	v_or_b32_e32 v45, 0x200, v0
	v_or_b32_e32 v46, 0x600, v0
	v_or_b32_e32 v47, 0xa00, v0
	v_or_b32_e32 v48, 0xe00, v0
	v_lshlrev_b32_e32 v34, 15, v76
	v_mov_b32_e32 v35, v71
	v_lshl_add_u64 v[34:35], s[8:9], 0, v[34:35]
	v_lshlrev_b32_e32 v36, 4, v73
	v_mov_b32_e32 v37, v71
	v_lshl_add_u64 v[68:69], v[34:35], 0, v[36:37]
	s_movk_i32 s0, 0x5000
	v_add_co_u32_e32 v38, vcc, s0, v68
	s_movk_i32 s0, 0x4000
	s_nop 0
	v_addc_co_u32_e32 v39, vcc, 0, v69, vcc
	global_load_dwordx4 v[34:37], v[68:69], off
	global_load_dwordx4 v[78:81], v[38:39], off offset:-4096
	v_add_co_u32_e32 v40, vcc, s0, v68
	s_nop 1
	v_addc_co_u32_e32 v41, vcc, 0, v69, vcc
	global_load_dwordx4 v[82:85], v[68:69], off offset:1024
	global_load_dwordx4 v[86:89], v[40:41], off offset:1024
	global_load_dwordx4 v[90:93], v[68:69], off offset:2048
	global_load_dwordx4 v[94:97], v[40:41], off offset:2048
	global_load_dwordx4 v[98:101], v[68:69], off offset:3072
	global_load_dwordx4 v[102:105], v[40:41], off offset:3072
	v_add_co_u32_e32 v74, vcc, s14, v68
	s_movk_i32 s0, 0x1000
	s_nop 0
	v_addc_co_u32_e32 v75, vcc, 0, v69, vcc
	global_load_dwordx4 v[106:109], v[74:75], off offset:-4096
	global_load_dwordx4 v[110:113], v[38:39], off
	v_add_co_u32_e32 v40, vcc, s0, v68
	s_nop 1
	v_addc_co_u32_e32 v41, vcc, 0, v69, vcc
	global_load_dwordx4 v[114:117], v[40:41], off offset:1024
	global_load_dwordx4 v[118:121], v[38:39], off offset:1024
	global_load_dwordx4 v[122:125], v[40:41], off offset:2048
	global_load_dwordx4 v[126:129], v[38:39], off offset:2048
	global_load_dwordx4 v[130:133], v[40:41], off offset:3072
	global_load_dwordx4 v[134:137], v[38:39], off offset:3072
	v_lshlrev_b32_e32 v38, 3, v0
	v_and_b32_e32 v38, 0x1f8, v38
	v_add_u32_e32 v38, 0, v38
	s_movk_i32 s0, 0x210
	s_waitcnt vmcnt(17)
	v_cvt_pk_f16_f32 v29, v28, v29
	v_cvt_pk_f16_f32 v28, v26, v27
	v_mad_u32_u24 v26, v76, s0, v38
	ds_write_b64 v26, v[28:29]
	v_lshrrev_b32_e32 v26, 6, v45
	v_cvt_pk_f16_f32 v5, v4, v5
	v_cvt_pk_f16_f32 v4, v2, v3
	v_mad_u32_u24 v2, v26, s0, v38
	ds_write_b64 v2, v[4:5]
	v_lshrrev_b32_e32 v4, 6, v42
	v_cvt_pk_f16_f32 v3, v8, v9
	v_cvt_pk_f16_f32 v2, v6, v7
	v_mad_u32_u24 v4, v4, s0, v38
	ds_write_b64 v4, v[2:3]
	v_lshrrev_b32_e32 v4, 6, v46
	v_cvt_pk_f16_f32 v3, v12, v13
	v_cvt_pk_f16_f32 v2, v10, v11
	v_mad_u32_u24 v4, v4, s0, v38
	ds_write_b64 v4, v[2:3]
	v_lshrrev_b32_e32 v4, 6, v43
	v_cvt_pk_f16_f32 v3, v16, v17
	v_cvt_pk_f16_f32 v2, v14, v15
	v_mad_u32_u24 v4, v4, s0, v38
	ds_write_b64 v4, v[2:3]
	v_lshrrev_b32_e32 v4, 6, v47
	v_cvt_pk_f16_f32 v3, v20, v21
	v_cvt_pk_f16_f32 v2, v18, v19
	v_mad_u32_u24 v4, v4, s0, v38
	ds_write_b64 v4, v[2:3]
	v_lshrrev_b32_e32 v4, 6, v44
	v_cvt_pk_f16_f32 v3, v24, v25
	v_cvt_pk_f16_f32 v2, v22, v23
	v_mad_u32_u24 v4, v4, s0, v38
	ds_write_b64 v4, v[2:3]
	v_lshrrev_b32_e32 v4, 6, v48
	s_waitcnt vmcnt(16)
	v_cvt_pk_f16_f32 v3, v32, v33
	v_cvt_pk_f16_f32 v2, v30, v31
	v_mad_u32_u24 v4, v4, s0, v38
	ds_write_b64 v4, v[2:3]
	v_mul_u32_u24_e32 v2, 0x210, v1
	v_lshlrev_b32_e32 v66, 4, v77
	v_add3_u32 v67, 0, v2, v66
	s_waitcnt lgkmcnt(0)
	s_barrier
	ds_read_b128 v[2:5], v67
	ds_read_b128 v[138:141], v67 offset:32
	ds_read_b128 v[6:9], v67 offset:16896
	ds_read_b128 v[142:145], v67 offset:16928
	s_movk_i32 s0, 0x7000
	v_add_co_u32_e32 v166, vcc, s0, v68
	s_waitcnt vmcnt(15) lgkmcnt(3)
	v_mfma_f32_32x32x16_f16 v[50:65], v[34:37], v[2:5], 0
	v_addc_co_u32_e32 v167, vcc, 0, v69, vcc
	global_load_dwordx4 v[146:149], v[74:75], off
	global_load_dwordx4 v[150:153], v[166:167], off offset:-4096
	ds_read_b128 v[154:157], v67 offset:64
	ds_read_b128 v[158:161], v67 offset:16960
	v_add_co_u32_e32 v168, vcc, s3, v68
	s_waitcnt lgkmcnt(3)
	v_mfma_f32_32x32x16_f16 v[34:49], v[34:37], v[6:9], 0
	v_addc_co_u32_e32 v169, vcc, 0, v69, vcc
	s_waitcnt vmcnt(16)
	v_mfma_f32_32x32x16_f16 v[18:33], v[78:81], v[2:5], 0
	v_mfma_f32_32x32x16_f16 v[2:17], v[78:81], v[6:9], 0
	s_waitcnt vmcnt(15)
	v_mfma_f32_32x32x16_f16 v[50:65], v[82:85], v[138:141], v[50:65]
	s_waitcnt lgkmcnt(2)
	v_mfma_f32_32x32x16_f16 v[34:49], v[82:85], v[142:145], v[34:49]
	global_load_dwordx4 v[78:81], v[74:75], off offset:1024
	global_load_dwordx4 v[82:85], v[168:169], off offset:1024
	s_waitcnt vmcnt(16)
	v_mfma_f32_32x32x16_f16 v[2:17], v[86:89], v[142:145], v[2:17]
	v_mfma_f32_32x32x16_f16 v[18:33], v[86:89], v[138:141], v[18:33]
	ds_read_b128 v[138:141], v67 offset:96
	ds_read_b128 v[162:165], v67 offset:16992
	s_waitcnt vmcnt(15) lgkmcnt(3)
	v_mfma_f32_32x32x16_f16 v[50:65], v[90:93], v[154:157], v[50:65]
	s_waitcnt lgkmcnt(2)
	v_mfma_f32_32x32x16_f16 v[34:49], v[90:93], v[158:161], v[34:49]
	global_load_dwordx4 v[86:89], v[74:75], off offset:2048
	global_load_dwordx4 v[90:93], v[168:169], off offset:2048
	s_waitcnt vmcnt(16)
	v_mfma_f32_32x32x16_f16 v[2:17], v[94:97], v[158:161], v[2:17]
	v_mfma_f32_32x32x16_f16 v[18:33], v[94:97], v[154:157], v[18:33]
	ds_read_b128 v[142:145], v67 offset:128
	ds_read_b128 v[154:157], v67 offset:17024
	s_waitcnt vmcnt(15) lgkmcnt(3)
	v_mfma_f32_32x32x16_f16 v[50:65], v[98:101], v[138:141], v[50:65]
	s_waitcnt lgkmcnt(2)
	v_mfma_f32_32x32x16_f16 v[34:49], v[98:101], v[162:165], v[34:49]
	global_load_dwordx4 v[94:97], v[74:75], off offset:3072
	global_load_dwordx4 v[98:101], v[168:169], off offset:3072
	s_waitcnt vmcnt(16)
	v_mfma_f32_32x32x16_f16 v[2:17], v[102:105], v[162:165], v[2:17]
	v_mfma_f32_32x32x16_f16 v[18:33], v[102:105], v[138:141], v[18:33]
	ds_read_b128 v[138:141], v67 offset:160
	ds_read_b128 v[158:161], v67 offset:17056
	s_movk_i32 s0, 0x3000
	v_add_co_u32_e32 v68, vcc, s0, v68
	s_waitcnt vmcnt(15) lgkmcnt(3)
	v_mfma_f32_32x32x16_f16 v[50:65], v[106:109], v[142:145], v[50:65]
	v_addc_co_u32_e32 v69, vcc, 0, v69, vcc
	s_waitcnt lgkmcnt(2)
	v_mfma_f32_32x32x16_f16 v[34:49], v[106:109], v[154:157], v[34:49]
	global_load_dwordx4 v[102:105], v[68:69], off
	global_load_dwordx4 v[106:109], v[166:167], off
	s_waitcnt vmcnt(16)
	v_mfma_f32_32x32x16_f16 v[2:17], v[110:113], v[154:157], v[2:17]
	v_mfma_f32_32x32x16_f16 v[18:33], v[110:113], v[142:145], v[18:33]
	ds_read_b128 v[142:145], v67 offset:192
	ds_read_b128 v[162:165], v67 offset:17088
	s_waitcnt vmcnt(15) lgkmcnt(3)
	v_mfma_f32_32x32x16_f16 v[50:65], v[114:117], v[138:141], v[50:65]
	s_waitcnt lgkmcnt(2)
	v_mfma_f32_32x32x16_f16 v[34:49], v[114:117], v[158:161], v[34:49]
	global_load_dwordx4 v[110:113], v[68:69], off offset:1024
	global_load_dwordx4 v[114:117], v[166:167], off offset:1024
	s_waitcnt vmcnt(16)
	v_mfma_f32_32x32x16_f16 v[2:17], v[118:121], v[158:161], v[2:17]
	v_mfma_f32_32x32x16_f16 v[18:33], v[118:121], v[138:141], v[18:33]
	ds_read_b128 v[138:141], v67 offset:224
	ds_read_b128 v[154:157], v67 offset:17120
	s_waitcnt vmcnt(15) lgkmcnt(3)
	v_mfma_f32_32x32x16_f16 v[50:65], v[122:125], v[142:145], v[50:65]
	s_waitcnt lgkmcnt(2)
	v_mfma_f32_32x32x16_f16 v[34:49], v[122:125], v[162:165], v[34:49]
	global_load_dwordx4 v[118:121], v[68:69], off offset:2048
	global_load_dwordx4 v[122:125], v[166:167], off offset:2048
	s_waitcnt vmcnt(16)
	v_mfma_f32_32x32x16_f16 v[2:17], v[126:129], v[162:165], v[2:17]
	v_mfma_f32_32x32x16_f16 v[18:33], v[126:129], v[142:145], v[18:33]
	ds_read_b128 v[142:145], v67 offset:256
	ds_read_b128 v[158:161], v67 offset:17152
	s_waitcnt vmcnt(15) lgkmcnt(3)
	v_mfma_f32_32x32x16_f16 v[50:65], v[130:133], v[138:141], v[50:65]
	s_waitcnt lgkmcnt(2)
	v_mfma_f32_32x32x16_f16 v[34:49], v[130:133], v[154:157], v[34:49]
	global_load_dwordx4 v[126:129], v[68:69], off offset:3072
	global_load_dwordx4 v[130:133], v[166:167], off offset:3072
	s_waitcnt vmcnt(16)
	v_mfma_f32_32x32x16_f16 v[2:17], v[134:137], v[154:157], v[2:17]
	v_mfma_f32_32x32x16_f16 v[18:33], v[134:137], v[138:141], v[18:33]
	ds_read_b128 v[138:141], v67 offset:288
	ds_read_b128 v[162:165], v67 offset:17184
	s_waitcnt vmcnt(14) lgkmcnt(2)
	v_mfma_f32_32x32x16_f16 v[2:17], v[150:153], v[158:161], v[2:17]
	v_mfma_f32_32x32x16_f16 v[50:65], v[146:149], v[142:145], v[50:65]
	v_mfma_f32_32x32x16_f16 v[18:33], v[150:153], v[142:145], v[18:33]
	ds_read_b128 v[134:137], v67 offset:320
	ds_read_b128 v[142:145], v67 offset:17216
	v_mfma_f32_32x32x16_f16 v[34:49], v[146:149], v[158:161], v[34:49]
	s_waitcnt vmcnt(12) lgkmcnt(2)
	v_mfma_f32_32x32x16_f16 v[2:17], v[82:85], v[162:165], v[2:17]
	v_mfma_f32_32x32x16_f16 v[50:65], v[78:81], v[138:141], v[50:65]
	v_mfma_f32_32x32x16_f16 v[34:49], v[78:81], v[162:165], v[34:49]
	v_mfma_f32_32x32x16_f16 v[18:33], v[82:85], v[138:141], v[18:33]
	ds_read_b128 v[78:81], v67 offset:352
	ds_read_b128 v[138:141], v67 offset:17248
	s_waitcnt vmcnt(10) lgkmcnt(2)
	v_mfma_f32_32x32x16_f16 v[2:17], v[90:93], v[142:145], v[2:17]
	v_mfma_f32_32x32x16_f16 v[50:65], v[86:89], v[134:137], v[50:65]
	v_mfma_f32_32x32x16_f16 v[34:49], v[86:89], v[142:145], v[34:49]
	ds_read_b128 v[82:85], v67 offset:384
	ds_read_b128 v[86:89], v67 offset:17280
	v_mfma_f32_32x32x16_f16 v[18:33], v[90:93], v[134:137], v[18:33]
	s_waitcnt vmcnt(8) lgkmcnt(2)
	v_mfma_f32_32x32x16_f16 v[2:17], v[98:101], v[138:141], v[2:17]
	v_mfma_f32_32x32x16_f16 v[50:65], v[94:97], v[78:81], v[50:65]
	v_mfma_f32_32x32x16_f16 v[18:33], v[98:101], v[78:81], v[18:33]
	ds_read_b128 v[78:81], v67 offset:416
	ds_read_b128 v[90:93], v67 offset:17312
	v_mfma_f32_32x32x16_f16 v[34:49], v[94:97], v[138:141], v[34:49]
	s_waitcnt vmcnt(6) lgkmcnt(2)
	v_mfma_f32_32x32x16_f16 v[2:17], v[106:109], v[86:89], v[2:17]
	v_mfma_f32_32x32x16_f16 v[50:65], v[102:105], v[82:85], v[50:65]
	v_mfma_f32_32x32x16_f16 v[18:33], v[106:109], v[82:85], v[18:33]
	ds_read_b128 v[82:85], v67 offset:448
	ds_read_b128 v[94:97], v67 offset:17344
	v_mfma_f32_32x32x16_f16 v[34:49], v[102:105], v[86:89], v[34:49]
	s_waitcnt vmcnt(4) lgkmcnt(2)
	v_mfma_f32_32x32x16_f16 v[2:17], v[114:117], v[90:93], v[2:17]
	v_mfma_f32_32x32x16_f16 v[50:65], v[110:113], v[78:81], v[50:65]
	v_mfma_f32_32x32x16_f16 v[18:33], v[114:117], v[78:81], v[18:33]
	ds_read_b128 v[78:81], v67 offset:480
	ds_read_b128 v[86:89], v67 offset:17376
	v_mfma_f32_32x32x16_f16 v[34:49], v[110:113], v[90:93], v[34:49]
	s_waitcnt vmcnt(2) lgkmcnt(2)
	v_mfma_f32_32x32x16_f16 v[2:17], v[122:125], v[94:97], v[2:17]
	v_mfma_f32_32x32x16_f16 v[50:65], v[118:121], v[82:85], v[50:65]
	v_mfma_f32_32x32x16_f16 v[34:49], v[118:121], v[94:97], v[34:49]
	v_mfma_f32_32x32x16_f16 v[18:33], v[122:125], v[82:85], v[18:33]
	s_waitcnt vmcnt(0) lgkmcnt(0)
	v_mfma_f32_32x32x16_f16 v[2:17], v[130:133], v[86:89], v[2:17]
	v_mfma_f32_32x32x16_f16 v[50:65], v[126:129], v[78:81], v[50:65]
	v_mfma_f32_32x32x16_f16 v[34:49], v[126:129], v[86:89], v[34:49]
	v_mfma_f32_32x32x16_f16 v[18:33], v[130:133], v[78:81], v[18:33]
	v_and_b32_e32 v98, 0x1c0, v0
	v_and_b32_e32 v67, 0xc0, v0
	v_lshlrev_b32_e32 v74, 2, v98
	v_mov_b32_e32 v75, v71
	s_movk_i32 s0, 0xfc00
	s_movk_i32 s3, 0x100
	v_lshlrev_b32_e32 v68, 2, v67
	v_mov_b32_e32 v69, v71
	v_lshl_add_u64 v[74:75], s[4:5], 0, v[74:75]
	s_mov_b32 s1, -1
	v_lshl_add_u64 v[68:69], s[10:11], 0, v[68:69]
	v_lshl_add_u64 v[74:75], v[74:75], 0, s[0:1]
	v_mov_b32_e32 v67, 0x3ed96d27
	v_cmp_gt_u32_e32 vcc, s3, v0
	s_barrier
	s_nop 0
	v_cndmask_b32_e32 v72, 1.0, v67, vcc
	v_cndmask_b32_e32 v69, v75, v69, vcc
	v_cndmask_b32_e32 v68, v74, v68, vcc
	v_mov_b32_e32 v67, v71
	v_lshl_add_u64 v[74:75], v[68:69], 0, v[66:67]
	s_movk_i32 s0, 0x90
	v_mad_u32_u24 v71, v98, s0, 0
	v_lshlrev_b32_e32 v77, 3, v77
	v_mul_u32_u24_e32 v1, 0x90, v1
	v_add3_u32 v77, v71, v77, v1
	s_movk_i32 s0, 0xff
	v_add_u32_e32 v106, 0x1000, v77
	v_cmp_lt_u32_e64 s[0:1], s0, v0
	s_lshr_b32 s3, s2, 3
	s_and_b32 s3, s3, 0x3ffc
	s_lshl_b32 s2, s2, 13
	s_and_b32 s2, s2, 0x3e000
	s_waitcnt vmcnt(7)
	v_pk_add_f32 v[50:51], v[172:173], v[50:51]
	v_pk_add_f32 v[52:53], v[174:175], v[52:53]
	s_waitcnt vmcnt(6)
	v_pk_add_f32 v[54:55], v[176:177], v[54:55]
	v_pk_add_f32 v[56:57], v[178:179], v[56:57]
	s_waitcnt vmcnt(3)
	v_pk_add_f32 v[18:19], v[188:189], v[18:19]
	v_pk_add_f32 v[20:21], v[190:191], v[20:21]
	v_pk_add_f32 v[2:3], v[188:189], v[2:3]
	v_pk_add_f32 v[4:5], v[190:191], v[4:5]
	v_pk_mul_f32 v[18:19], v[72:73], v[18:19] op_sel_hi:[0,1]
	v_pk_mul_f32 v[20:21], v[72:73], v[20:21] op_sel_hi:[0,1]
	v_pk_mul_f32 v[2:3], v[72:73], v[2:3] op_sel_hi:[0,1]
	v_pk_mul_f32 v[4:5], v[72:73], v[4:5] op_sel_hi:[0,1]
	v_cvt_pk_f16_f32 v18, v18, v19
	v_cvt_pk_f16_f32 v19, v20, v21
	v_cvt_pk_f16_f32 v2, v2, v3
	v_cvt_pk_f16_f32 v3, v4, v5
	s_waitcnt vmcnt(2)
	v_pk_add_f32 v[4:5], v[192:193], v[22:23]
	v_pk_add_f32 v[20:21], v[194:195], v[24:25]
	v_pk_add_f32 v[58:59], v[180:181], v[58:59]
	v_pk_add_f32 v[60:61], v[182:183], v[60:61]
	v_pk_add_f32 v[62:63], v[184:185], v[62:63]
	v_pk_add_f32 v[64:65], v[186:187], v[64:65]
	v_pk_add_f32 v[34:35], v[172:173], v[34:35]
	v_pk_add_f32 v[36:37], v[174:175], v[36:37]
	v_pk_add_f32 v[38:39], v[176:177], v[38:39]
	v_pk_add_f32 v[40:41], v[178:179], v[40:41]
	v_pk_mul_f32 v[50:51], v[72:73], v[50:51] op_sel_hi:[0,1]
	v_pk_mul_f32 v[52:53], v[72:73], v[52:53] op_sel_hi:[0,1]
	v_pk_mul_f32 v[54:55], v[72:73], v[54:55] op_sel_hi:[0,1]
	v_pk_mul_f32 v[56:57], v[72:73], v[56:57] op_sel_hi:[0,1]
	v_pk_mul_f32 v[4:5], v[72:73], v[4:5] op_sel_hi:[0,1]
	v_pk_mul_f32 v[20:21], v[72:73], v[20:21] op_sel_hi:[0,1]
	v_pk_mul_f32 v[34:35], v[72:73], v[34:35] op_sel_hi:[0,1]
	v_pk_mul_f32 v[36:37], v[72:73], v[36:37] op_sel_hi:[0,1]
	v_pk_mul_f32 v[38:39], v[72:73], v[38:39] op_sel_hi:[0,1]
	v_pk_mul_f32 v[40:41], v[72:73], v[40:41] op_sel_hi:[0,1]
	v_pk_mul_f32 v[58:59], v[72:73], v[58:59] op_sel_hi:[0,1]
	v_pk_mul_f32 v[60:61], v[72:73], v[60:61] op_sel_hi:[0,1]
	v_pk_mul_f32 v[62:63], v[72:73], v[62:63] op_sel_hi:[0,1]
	v_pk_mul_f32 v[64:65], v[72:73], v[64:65] op_sel_hi:[0,1]
	v_cvt_pk_f16_f32 v50, v50, v51
	v_cvt_pk_f16_f32 v51, v52, v53
	v_cvt_pk_f16_f32 v52, v54, v55
	v_cvt_pk_f16_f32 v53, v56, v57
	v_cvt_pk_f16_f32 v4, v4, v5
	v_cvt_pk_f16_f32 v5, v20, v21
	v_cvt_pk_f16_f32 v34, v34, v35
	v_cvt_pk_f16_f32 v35, v36, v37
	v_cvt_pk_f16_f32 v36, v38, v39
	v_cvt_pk_f16_f32 v37, v40, v41
	v_cvt_pk_f16_f32 v38, v58, v59
	v_cvt_pk_f16_f32 v39, v60, v61
	v_cvt_pk_f16_f32 v40, v62, v63
	v_cvt_pk_f16_f32 v41, v64, v65
	ds_write2_b64 v77, v[50:51], v[52:53] offset1:2
	ds_write2_b64 v106, v[34:35], v[36:37] offset0:64 offset1:66
	ds_write2_b64 v77, v[38:39], v[40:41] offset0:4 offset1:6
	ds_write2_b64 v77, v[18:19], v[4:5] offset0:8 offset1:10
	v_pk_add_f32 v[0:1], v[192:193], v[6:7]
	v_pk_add_f32 v[4:5], v[194:195], v[8:9]
	v_pk_mul_f32 v[0:1], v[72:73], v[0:1] op_sel_hi:[0,1]
	v_pk_mul_f32 v[4:5], v[72:73], v[4:5] op_sel_hi:[0,1]
	v_cvt_pk_f16_f32 v0, v0, v1
	v_cvt_pk_f16_f32 v1, v4, v5
	ds_write2_b64 v106, v[2:3], v[0:1] offset0:72 offset1:74
	s_waitcnt vmcnt(1)
	v_pk_add_f32 v[0:1], v[196:197], v[26:27]
	v_pk_add_f32 v[2:3], v[198:199], v[28:29]
	v_pk_mul_f32 v[0:1], v[72:73], v[0:1] op_sel_hi:[0,1]
	v_pk_mul_f32 v[2:3], v[72:73], v[2:3] op_sel_hi:[0,1]
	v_cvt_pk_f16_f32 v0, v0, v1
	v_cvt_pk_f16_f32 v1, v2, v3
	v_pk_add_f32 v[2:3], v[196:197], v[10:11]
	v_pk_add_f32 v[4:5], v[198:199], v[12:13]
	v_pk_mul_f32 v[2:3], v[72:73], v[2:3] op_sel_hi:[0,1]
	v_pk_mul_f32 v[4:5], v[72:73], v[4:5] op_sel_hi:[0,1]
	v_cvt_pk_f16_f32 v2, v2, v3
	v_cvt_pk_f16_f32 v3, v4, v5
	s_waitcnt vmcnt(0)
	v_pk_add_f32 v[4:5], v[200:201], v[30:31]
	v_pk_add_f32 v[6:7], v[202:203], v[32:33]
	v_pk_mul_f32 v[4:5], v[72:73], v[4:5] op_sel_hi:[0,1]
	v_pk_mul_f32 v[6:7], v[72:73], v[6:7] op_sel_hi:[0,1]
	v_cvt_pk_f16_f32 v4, v4, v5
	v_cvt_pk_f16_f32 v5, v6, v7
	ds_write2_b64 v77, v[0:1], v[4:5] offset0:12 offset1:14
	v_pk_add_f32 v[0:1], v[200:201], v[14:15]
	v_pk_add_f32 v[4:5], v[202:203], v[16:17]
	v_pk_mul_f32 v[0:1], v[72:73], v[0:1] op_sel_hi:[0,1]
	v_pk_mul_f32 v[4:5], v[72:73], v[4:5] op_sel_hi:[0,1]
	v_cvt_pk_f16_f32 v0, v0, v1
	v_cvt_pk_f16_f32 v1, v4, v5
	ds_write2_b64 v106, v[2:3], v[0:1] offset0:76 offset1:78
	v_mov_b32_e32 v0, s12
	v_mov_b32_e32 v1, s6
	v_pk_add_f32 v[42:43], v[180:181], v[42:43]
	v_pk_add_f32 v[44:45], v[182:183], v[44:45]
	v_pk_add_f32 v[46:47], v[184:185], v[46:47]
	v_pk_add_f32 v[48:49], v[186:187], v[48:49]
	v_cndmask_b32_e32 v0, v0, v1, vcc
	v_mov_b32_e32 v1, s13
	v_mov_b32_e32 v2, s7
	v_and_or_b32 v4, v76, 3, s3
	v_pk_mul_f32 v[42:43], v[72:73], v[42:43] op_sel_hi:[0,1]
	v_pk_mul_f32 v[44:45], v[72:73], v[44:45] op_sel_hi:[0,1]
	v_pk_mul_f32 v[46:47], v[72:73], v[46:47] op_sel_hi:[0,1]
	v_pk_mul_f32 v[48:49], v[72:73], v[48:49] op_sel_hi:[0,1]
	v_cndmask_b32_e32 v1, v1, v2, vcc
	v_lshl_or_b32 v4, v4, 18, s2
	v_cvt_pk_f16_f32 v42, v42, v43
	v_cvt_pk_f16_f32 v43, v44, v45
	v_cvt_pk_f16_f32 v44, v46, v47
	v_cvt_pk_f16_f32 v45, v48, v49
	v_and_b32_e32 v1, 0xffff, v1
	v_mov_b32_e32 v2, 0x800000
	v_mov_b32_e32 v3, 0x20000
	v_lshl_or_b32 v8, v73, 4, v4
	ds_write2_b64 v106, v[42:43], v[44:45] offset0:68 offset1:70
	s_waitcnt lgkmcnt(0)
	v_readfirstlane_b32 s4, v0
	v_readfirstlane_b32 s5, v1
	v_readfirstlane_b32 s8, v76
	s_mov_b32 s6, 0x800000
	s_mov_b32 s7, 0x20000
	v_add_u32_e32 v10, 0x1000, v8
	v_lshrrev_b32_e32 v4, 2, v73
	v_mul_u32_u24_e32 v4, 0x90, v4
	v_and_b32_e32 v5, 48, v70
	s_movk_i32 s0, 0x90
	s_cmp_lt_u32 s8, 4
	s_cbranch_scc1 .Lmy_proj_qk
	v_add3_u32 v9, v71, v4, v5
	ds_read_b128 v[12:15], v9
	ds_read_b128 v[16:19], v9 offset:2304
	ds_read_b128 v[20:23], v9 offset:4608
	ds_read_b128 v[24:27], v9 offset:6912
	ds_read_b128 v[28:31], v9 offset:64
	ds_read_b128 v[32:35], v9 offset:2368
	ds_read_b128 v[36:39], v9 offset:4672
	ds_read_b128 v[40:43], v9 offset:6976
	s_waitcnt lgkmcnt(7)
	buffer_store_dwordx4 v[12:15], v8, s[4:7], 0 offen sc1
	s_waitcnt lgkmcnt(6)
	buffer_store_dwordx4 v[16:19], v8, s[4:7], 0 offen offset:1024 sc1
	s_waitcnt lgkmcnt(5)
	buffer_store_dwordx4 v[20:23], v8, s[4:7], 0 offen offset:2048 sc1
	s_waitcnt lgkmcnt(4)
	buffer_store_dwordx4 v[24:27], v8, s[4:7], 0 offen offset:3072 sc1
	s_waitcnt lgkmcnt(3)
	buffer_store_dwordx4 v[28:31], v10, s[4:7], 0 offen sc1
	s_waitcnt lgkmcnt(2)
	buffer_store_dwordx4 v[32:35], v10, s[4:7], 0 offen offset:1024 sc1
	s_waitcnt lgkmcnt(1)
	buffer_store_dwordx4 v[36:39], v10, s[4:7], 0 offen offset:2048 sc1
	s_waitcnt lgkmcnt(0)
	buffer_store_dwordx4 v[40:43], v10, s[4:7], 0 offen offset:3072 sc1
	s_endpgm
.Lmy_proj_qk:
	v_mad_u32_u24 v9, v73, s0, v71
	ds_read_b128 v[12:15], v9
	ds_read_b128 v[16:19], v9 offset:16
	ds_read_b128 v[20:23], v9 offset:32
	ds_read_b128 v[24:27], v9 offset:48
	ds_read_b128 v[28:31], v9 offset:64
	ds_read_b128 v[32:35], v9 offset:80
	ds_read_b128 v[36:39], v9 offset:96
	ds_read_b128 v[40:43], v9 offset:112
	s_waitcnt lgkmcnt(7)
	buffer_store_dwordx4 v[12:15], v8, s[4:7], 0 offen sc1
	s_waitcnt lgkmcnt(6)
	buffer_store_dwordx4 v[16:19], v8, s[4:7], 0 offen offset:1024 sc1
	s_waitcnt lgkmcnt(5)
	buffer_store_dwordx4 v[20:23], v8, s[4:7], 0 offen offset:2048 sc1
	s_waitcnt lgkmcnt(4)
	buffer_store_dwordx4 v[24:27], v8, s[4:7], 0 offen offset:3072 sc1
	s_waitcnt lgkmcnt(3)
	buffer_store_dwordx4 v[28:31], v10, s[4:7], 0 offen sc1
	s_waitcnt lgkmcnt(2)
	buffer_store_dwordx4 v[32:35], v10, s[4:7], 0 offen offset:1024 sc1
	s_waitcnt lgkmcnt(1)
	buffer_store_dwordx4 v[36:39], v10, s[4:7], 0 offen offset:2048 sc1
	s_waitcnt lgkmcnt(0)
	buffer_store_dwordx4 v[40:43], v10, s[4:7], 0 offen offset:3072 sc1
	s_endpgm

	.amdhsa_kernel _Z11proj_kernelPKfS0_PKDF16_S0_S0_PDF16_S3_
		.amdhsa_group_segment_fixed_size 0
		.amdhsa_private_segment_fixed_size 0
		.amdhsa_kernarg_size 56
		.amdhsa_user_sgpr_count 2
		.amdhsa_user_sgpr_dispatch_ptr 0
		.amdhsa_user_sgpr_queue_ptr 0
		.amdhsa_user_sgpr_kernarg_segment_ptr 1
		.amdhsa_user_sgpr_dispatch_id 0
		.amdhsa_user_sgpr_kernarg_preload_length 0
		.amdhsa_user_sgpr_kernarg_preload_offset 0
		.amdhsa_user_sgpr_private_segment_size 0
		.amdhsa_uses_dynamic_stack 0
		.amdhsa_enable_private_segment 0
		.amdhsa_system_sgpr_workgroup_id_x 1
		.amdhsa_system_sgpr_workgroup_id_y 0
		.amdhsa_system_sgpr_workgroup_id_z 0
		.amdhsa_system_sgpr_workgroup_info 0
		.amdhsa_system_vgpr_workitem_id 0
		.amdhsa_next_free_vgpr 205
		.amdhsa_next_free_sgpr 20
		.amdhsa_accum_offset 208
		.amdhsa_reserve_vcc 1
		.amdhsa_float_round_mode_32 0
		.amdhsa_float_round_mode_16_64 0
		.amdhsa_float_denorm_mode_32 3
		.amdhsa_float_denorm_mode_16_64 3
		.amdhsa_dx10_clamp 1
		.amdhsa_ieee_mode 1
		.amdhsa_fp16_overflow 0
		.amdhsa_tg_split 0
		.amdhsa_exception_fp_ieee_invalid_op 0
		.amdhsa_exception_fp_denorm_src 0
		.amdhsa_exception_fp_ieee_div_zero 0
		.amdhsa_exception_fp_ieee_overflow 0
		.amdhsa_exception_fp_ieee_underflow 0
		.amdhsa_exception_fp_ieee_inexact 0
		.amdhsa_exception_int_div_zero 0
	.end_amdhsa_kernel

amdhsa.kernels:
  - .agpr_count:     0
    .args:
      - .actual_access:  read_only
        .address_space:  global
        .offset:         0
        .size:           8
        .value_kind:     global_buffer
      - .actual_access:  read_only
        .address_space:  global
        .offset:         8
        .size:           8
        .value_kind:     global_buffer
      - .actual_access:  read_only
        .address_space:  global
        .offset:         16
        .size:           8
        .value_kind:     global_buffer
      - .actual_access:  read_only
        .address_space:  global
        .offset:         24
        .size:           8
        .value_kind:     global_buffer
      - .actual_access:  read_only
        .address_space:  global
        .offset:         32
        .size:           8
        .value_kind:     global_buffer
      - .actual_access:  write_only
        .address_space:  global
        .offset:         40
        .size:           8
        .value_kind:     global_buffer
      - .actual_access:  write_only
        .address_space:  global
        .offset:         48
        .size:           8
        .value_kind:     global_buffer
      - .actual_access:  write_only
        .address_space:  global
        .offset:         56
        .size:           8
        .value_kind:     global_buffer
      - .actual_access:  write_only
        .address_space:  global
        .offset:         64
        .size:           8
        .value_kind:     global_buffer
    .group_segment_fixed_size: 0
    .kernarg_segment_align: 8
    .kernarg_segment_size: 72
    .language:       OpenCL C
    .language_version:
      - 2
      - 0
    .max_flat_workgroup_size: 256
    .name:           _Z11prep_kernelPKfS0_S0_S0_S0_PDF16_S1_S1_S1_
    .private_segment_fixed_size: 0
    .sgpr_count:     21
    .sgpr_spill_count: 0
    .symbol:         _Z11prep_kernelPKfS0_S0_S0_S0_PDF16_S1_S1_S1_.kd
    .uniform_work_group_size: 1
    .uses_dynamic_stack: false
    .vgpr_count:     18
    .vgpr_spill_count: 0
    .wavefront_size: 64
  - .agpr_count:     0
    .args:
      - .actual_access:  read_only
        .address_space:  global
        .offset:         0
        .size:           8
        .value_kind:     global_buffer
      - .actual_access:  read_only
        .address_space:  global
        .offset:         8
        .size:           8
        .value_kind:     global_buffer
      - .actual_access:  read_only
        .address_space:  global
        .offset:         16
        .size:           8
        .value_kind:     global_buffer
      - .actual_access:  read_only
        .address_space:  global
        .offset:         24
        .size:           8
        .value_kind:     global_buffer
      - .actual_access:  read_only
        .address_space:  global
        .offset:         32
        .size:           8
        .value_kind:     global_buffer
      - .actual_access:  write_only
        .address_space:  global
        .offset:         40
        .size:           8
        .value_kind:     global_buffer
      - .actual_access:  write_only
        .address_space:  global
        .offset:         48
        .size:           8
        .value_kind:     global_buffer
    .group_segment_fixed_size: 0
    .kernarg_segment_align: 8
    .kernarg_segment_size: 56
    .language:       OpenCL C
    .language_version:
      - 2
      - 0
    .max_flat_workgroup_size: 512
    .name:           _Z11proj_kernelPKfS0_PKDF16_S0_S0_PDF16_S3_
    .private_segment_fixed_size: 0
    .sgpr_count:     26
    .sgpr_spill_count: 0
    .symbol:         _Z11proj_kernelPKfS0_PKDF16_S0_S0_PDF16_S3_.kd
    .uniform_work_group_size: 1
    .uses_dynamic_stack: false
    .vgpr_count:     205
    .vgpr_spill_count: 0
    .wavefront_size: 64
  - .agpr_count:     0
    .args:
      - .address_space:  global
        .offset:         0
        .size:           8
        .value_kind:     global_buffer
      - .address_space:  global
        .offset:         8
        .size:           8
        .value_kind:     global_buffer
      - .actual_access:  write_only
        .address_space:  global
        .offset:         16
        .size:           8
        .value_kind:     global_buffer
    .group_segment_fixed_size: 0
    .kernarg_segment_align: 8
    .kernarg_segment_size: 24
    .language:       OpenCL C
    .language_version:
      - 2
      - 0
    .max_flat_workgroup_size: 512
    .name:           _Z11attn_kernelPKDF16_S0_PDF16_
    .private_segment_fixed_size: 0
    .sgpr_count:     42
    .sgpr_spill_count: 0
    .symbol:         _Z11attn_kernelPKDF16_S0_PDF16_.kd
    .uniform_work_group_size: 1
    .uses_dynamic_stack: false
    .vgpr_count:     197
    .vgpr_spill_count: 0
    .wavefront_size: 64
  - .agpr_count:     0
    .args:
      - .actual_access:  read_only
        .address_space:  global
        .offset:         0
        .size:           8
        .value_kind:     global_buffer
      - .actual_access:  read_only
        .address_space:  global
        .offset:         8
        .size:           8
        .value_kind:     global_buffer
      - .actual_access:  read_only
        .address_space:  global
        .offset:         16
        .size:           8
        .value_kind:     global_buffer
      - .actual_access:  read_only
        .address_space:  global
        .offset:         24
        .size:           8
        .value_kind:     global_buffer
      - .actual_access:  read_only
        .address_space:  global
        .offset:         32
        .size:           8
        .value_kind:     global_buffer
      - .address_space:  global
        .offset:         40
        .size:           8
        .value_kind:     global_buffer
      - .actual_access:  read_only
        .address_space:  global
        .offset:         48
        .size:           8
        .value_kind:     global_buffer
      - .actual_access:  read_only
        .address_space:  global
        .offset:         56
        .size:           8
        .value_kind:     global_buffer
      - .actual_access:  read_only
        .address_space:  global
        .offset:         64
        .size:           8
        .value_kind:     global_buffer
      - .address_space:  global
        .offset:         72
        .size:           8
        .value_kind:     global_buffer
      - .actual_access:  read_only
        .address_space:  global
        .offset:         80
        .size:           8
        .value_kind:     global_buffer
      - .actual_access:  write_only
        .address_space:  global
        .offset:         88
        .size:           8
        .value_kind:     global_buffer
    .group_segment_fixed_size: 0
    .kernarg_segment_align: 8
    .kernarg_segment_size: 96
    .language:       OpenCL C
    .language_version:
      - 2
      - 0
    .max_flat_workgroup_size: 512
    .name:           _Z10ffn_kernelPKfS0_PKDF16_S2_S0_S2_S0_S0_S0_S2_S0_Pf
    .private_segment_fixed_size: 0
    .sgpr_count:     24
    .sgpr_spill_count: 0
    .symbol:         _Z10ffn_kernelPKfS0_PKDF16_S2_S0_S2_S0_S0_S0_S2_S0_Pf.kd
    .uniform_work_group_size: 1
    .uses_dynamic_stack: false
    .vgpr_count:     230
    .vgpr_spill_count: 0
    .wavefront_size: 64
